# first K-iteration peeled with C=0 MFMAs (no accumulator zeroing); P23 acc[1] epilogue rows sunk into the next unit's first iteration
# baseline (speedup 1.0000x reference)
.LBB0_2926:
	s_add_u32 s12, s38, 0x4b400000
	v_mov_b32_e32 v3, v177
	s_addc_u32 s13, s39, 0
	s_waitcnt vmcnt(2)
	s_barrier
	s_or_b32 s18, s83, 0x80
	s_add_i32 s58, s49, 0x18000
	s_mov_b32 m0, s58
	v_add_u32_e32 v3, s18, v3
	global_load_lds_dwordx4 v3, s[6:7]
	v_mov_b32_e32 v3, v177
	s_add_i32 s18, s18, s48
	s_add_i32 s59, s49, 0x1a000
	v_add_u32_e32 v3, s18, v3
	s_mov_b32 m0, s59
	s_or_b32 s18, s82, 0x80
	global_load_lds_dwordx4 v3, s[6:7]
	v_mov_b32_e32 v3, v176
	s_add_i32 s60, s49, 0x8000
	v_add_u32_e32 v3, s18, v3
	s_mov_b32 m0, s60
	s_add_i32 s18, s18, s47
	global_load_lds_dwordx4 v3, s[4:5]
	v_mov_b32_e32 v3, v176
	s_add_i32 s61, s49, 0xa000
	s_lshl_b32 s17, s17, 8
	v_add_u32_e32 v3, s18, v3
	s_mov_b32 m0, s61
	s_add_i32 s17, s83, s17
	global_load_lds_dwordx4 v3, s[4:5]
	v_mov_b32_e32 v3, v177
	s_addk_i32 s17, 0x80
	s_add_i32 s62, s49, 0x1c000
	s_mov_b32 m0, s62
	v_add_u32_e32 v3, s17, v3
	global_load_lds_dwordx4 v3, s[6:7]
	v_mov_b32_e32 v3, v177
	s_add_i32 s17, s17, s48
	s_add_i32 s63, s49, 0x1e000
	v_add_u32_e32 v3, s17, v3
	s_mov_b32 m0, s63
	s_ashr_i32 s17, s14, 31
	global_load_lds_dwordx4 v3, s[6:7]
	s_and_b32 s15, s15, 3
	s_lshr_b32 s17, s17, 26
	v_and_b32_e32 v178, 15, v2
	v_bfe_u32 v179, v2, 4, 2
	s_add_i32 s17, s14, s17
	s_lshl_b32 s66, s8, 6
	v_and_b32_e32 v3, 48, v2
	s_lshl_b32 s18, s8, 13
	s_lshl_b32 s8, s15, 5
	s_lshl_b32 s15, s15, 12
	v_lshlrev_b32_e32 v2, 2, v2
	s_ashr_i32 s64, s17, 6
	s_lshl_b32 s65, s70, 8
	v_lshlrev_b32_e32 v4, 6, v178
	v_and_b32_e32 v2, 32, v2
	s_add_i32 s15, s15, 0
	v_bitop3_b32 v2, v4, v2, v3 bitop3:0x36
	s_cmp_gt_i32 s14, 63
	v_add_u32_e32 v3, 0, v2
	v_add_u32_e32 v2, s15, v2
	s_waitcnt vmcnt(6)
	s_cselect_b64 s[14:15], -1, 0
	s_add_i32 s67, s64, -2
	s_cmpk_lt_u32 s16, 0x100
	v_add_u32_e32 v180, 0x10000, v2
	v_add_u32_e32 v181, 0x10400, v2
	v_add_u32_e32 v182, 0x14000, v2
	v_add_u32_e32 v183, 0x14400, v2
	v_add_u32_e32 v184, 0x18000, v2
	v_add_u32_e32 v185, 0x18400, v2
	v_add_u32_e32 v186, 0x1c000, v2
	v_add_u32_e32 v187, 0x1c400, v2
	s_cselect_b64 s[16:17], -1, 0
	s_ashr_i32 s68, s66, 31
	v_add_u32_e32 v188, 0x10800, v2
	v_add_u32_e32 v189, 0x10c00, v2
	v_add_u32_e32 v190, 0x14800, v2
	v_add_u32_e32 v191, 0x14c00, v2
	v_add_u32_e32 v192, 0x18800, v2
	v_add_u32_e32 v193, 0x18c00, v2
	v_add_u32_e32 v194, 0x1c800, v2
	v_add_u32_e32 v195, 0x1cc00, v2
	s_ashr_i32 s69, s34, 31
	s_mulk_i32 s70, 0x180
	v_mov_b64_e32 v[162:163], s[2:3]
	v_add_u32_e32 v196, s18, v3
	s_mov_b32 s18, 0x39000000
	s_mov_b32 s20, 0x3a800000
	s_movk_i32 s71, 0x1600
	s_mov_b32 s72, 0xc3e00000
	s_mov_b32 s73, 0x2c000
	s_mov_b32 s74, 0x42000
	s_mov_b32 s75, 0xb0000
	s_mov_b32 s76, 0xc6000
	s_mov_b32 s77, 0xdc000
	v_mov_b32_e32 v197, 0x43e00000
	s_mov_b32 s78, s9
	s_mov_b32 s99, 0
	s_barrier
	s_branch .LBB0_2929

.LBB0_2934:
	s_ashr_i32 s22, s25, 3
	s_add_i32 s22, s29, s22
	s_mul_hi_i32 s23, s22, 0x2e8ba2e9
	s_lshr_b32 s25, s23, 31
	s_ashr_i32 s23, s23, 6
	s_add_i32 s23, s23, s25
	s_lshl_b32 s25, s23, 3
	s_sub_i32 s28, s19, s25
	s_min_i32 s28, s28, 8
	s_abs_i32 s29, s28
	v_cvt_f32_u32_e32 v2, s29
	s_sub_i32 s80, 0, s29
	s_mulk_i32 s23, 0x160
	s_sub_i32 s22, s22, s23
	v_rcp_iflag_f32_e32 v2, v2
	s_abs_i32 s23, s22
	s_xor_b32 s79, s22, s28
	s_ashr_i32 s79, s79, 31
	v_mul_f32_e32 v2, 0x4f7ffffe, v2
	v_cvt_u32_f32_e32 v2, v2
	s_nop 0
	v_readfirstlane_b32 s84, v2
	s_mul_i32 s80, s80, s84
	s_mul_hi_u32 s80, s84, s80
	s_add_i32 s84, s84, s80
	s_mul_hi_u32 s80, s23, s84
	s_mul_i32 s84, s80, s29
	s_sub_i32 s23, s23, s84
	s_add_i32 s85, s80, 1
	s_sub_i32 s84, s23, s29
	s_cmp_ge_u32 s23, s29
	s_cselect_b32 s80, s85, s80
	s_cselect_b32 s23, s84, s23
	s_add_i32 s84, s80, 1
	s_cmp_ge_u32 s23, s29
	s_cselect_b32 s23, s84, s80
	s_xor_b32 s23, s23, s79
	s_sub_i32 s79, s23, s79
	s_mul_i32 s23, s79, s28
	s_sub_i32 s22, s22, s23
	s_add_i32 s22, s25, s22
	s_ashr_i32 s23, s22, 31
	s_lshl_b32 s80, s22, 19
	s_lshl_b64 s[28:29], s[22:23], 2
	s_add_u32 s28, s45, s28
	s_addc_u32 s29, s46, s29
	global_load_dword v209, v1, s[28:29]
	s_mov_b32 s25, s80
.LBB0_2935:
	s_andn2_b64 vcc, exec, s[14:15]
	v_mov_b64_e32 v[2:3], 0
	v_mov_b64_e32 v[4:5], 0
	v_mov_b64_e32 v[6:7], 0
	v_mov_b64_e32 v[8:9], 0
	v_mov_b64_e32 v[10:11], 0
	v_mov_b64_e32 v[12:13], 0
	v_mov_b64_e32 v[14:15], 0
	v_mov_b64_e32 v[16:17], 0
	v_mov_b64_e32 v[18:19], 0
	v_mov_b64_e32 v[20:21], 0
	v_mov_b64_e32 v[22:23], 0
	v_mov_b64_e32 v[24:25], 0
	v_mov_b64_e32 v[26:27], 0
	v_mov_b64_e32 v[28:29], 0
	v_mov_b64_e32 v[30:31], 0
	v_mov_b64_e32 v[32:33], 0
	v_mov_b64_e32 v[164:165], 0
	v_mov_b64_e32 v[166:167], 0
	v_mov_b64_e32 v[168:169], 0
	v_mov_b64_e32 v[170:171], 0
	v_mov_b64_e32 v[172:173], 0
	v_mov_b64_e32 v[174:175], 0
	s_cbranch_vccnz .Lzs_12
	s_add_i32 s28, s82, 0x80
	s_add_i32 s82, s83, 0x100
	s_mov_b32 s83, 0
	s_cmp_lg_u32 s99, 0
	s_cbranch_scc1 .Lsk23_first
	ds_read_b128 v[18:21], v180
	ds_read_b128 v[22:25], v181
	ds_read_b128 v[26:29], v188
	ds_read_b128 v[30:33], v189
	ds_read_b128 v[2:5], v182
	ds_read_b128 v[6:9], v183
	ds_read_b128 v[10:13], v190
	ds_read_b128 v[14:17], v191
	s_add_i32 s84, s28, 0x80
	s_cmp_eq_u32 s67, s83
	s_cselect_b32 s86, s25, s84
	s_cselect_b32 s87, s29, s82
	s_add_i32 s84, s86, 0x80
	s_add_i32 s85, s87, 0x80
	v_mov_b32_e32 v172, v176
	ds_read_b128 v[164:167], v196
	ds_read_b128 v[168:171], v196 offset:1024
	ds_read_b128 v[198:201], v196 offset:2048
	ds_read_b128 v[202:205], v196 offset:3072
	ds_read_b128 v[214:217], v196 offset:4096
	ds_read_b128 v[218:221], v196 offset:5120
	ds_read_b128 v[222:225], v196 offset:6144
	ds_read_b128 v[226:229], v196 offset:7168
	s_add_i32 s88, s28, s65
	v_add_u32_e32 v172, s88, v172
	s_add_i32 m0, s49, 0xc000
	s_add_i32 s88, s28, s70
	global_load_lds_dwordx4 v172, s[4:5]
	v_mov_b32_e32 v172, v176
	s_add_i32 m0, s49, 0xe000
	v_add_u32_e32 v172, s88, v172
	global_load_lds_dwordx4 v172, s[4:5]
	s_waitcnt vmcnt(8)
	s_waitcnt lgkmcnt(0)
	s_barrier
	s_setprio 1
	s_waitcnt lgkmcnt(0)
	v_mfma_f32_16x16x128_f8f6f4 v[158:161], v[18:25], v[164:171], 0
	v_mfma_f32_16x16x128_f8f6f4 v[154:157], v[26:33], v[164:171], 0
	v_mfma_f32_16x16x128_f8f6f4 v[150:153], v[18:25], v[198:205], 0
	v_mfma_f32_16x16x128_f8f6f4 v[146:149], v[26:33], v[198:205], 0
	v_mfma_f32_16x16x128_f8f6f4 v[138:141], v[18:25], v[214:221], 0
	v_mfma_f32_16x16x128_f8f6f4 v[130:133], v[26:33], v[214:221], 0
	v_mfma_f32_16x16x128_f8f6f4 v[122:125], v[18:25], v[222:229], 0
	v_mfma_f32_16x16x128_f8f6f4 v[114:117], v[26:33], v[222:229], 0
	s_setprio 0
	s_setprio 1
	v_mfma_f32_16x16x128_f8f6f4 v[142:145], v[2:9], v[164:171], 0
	v_mfma_f32_16x16x128_f8f6f4 v[134:137], v[10:17], v[164:171], 0
	v_mfma_f32_16x16x128_f8f6f4 v[126:129], v[2:9], v[198:205], 0
	v_mfma_f32_16x16x128_f8f6f4 v[118:121], v[10:17], v[198:205], 0
	v_mfma_f32_16x16x128_f8f6f4 v[110:113], v[2:9], v[214:221], 0
	v_mfma_f32_16x16x128_f8f6f4 v[106:109], v[10:17], v[214:221], 0
	v_mfma_f32_16x16x128_f8f6f4 v[102:105], v[2:9], v[222:229], 0
	v_mfma_f32_16x16x128_f8f6f4 v[98:101], v[10:17], v[222:229], 0
	s_setprio 0
	s_barrier
	v_mov_b32_e32 v172, v177
	ds_read_b128 v[164:167], v196 offset:16384
	ds_read_b128 v[168:171], v196 offset:17408
	ds_read_b128 v[198:201], v196 offset:18432
	ds_read_b128 v[202:205], v196 offset:19456
	ds_read_b128 v[214:217], v196 offset:20480
	ds_read_b128 v[218:221], v196 offset:21504
	ds_read_b128 v[222:225], v196 offset:22528
	ds_read_b128 v[226:229], v196 offset:23552
	s_mov_b32 m0, s50
	v_add_u32_e32 v172, s87, v172
	global_load_lds_dwordx4 v172, s[6:7]
	v_mov_b32_e32 v172, v177
	s_add_i32 s87, s87, s48
	v_add_u32_e32 v172, s87, v172
	s_mov_b32 m0, s51
	s_add_i32 s87, s87, s48
	global_load_lds_dwordx4 v172, s[6:7]
	v_mov_b32_e32 v172, v177
	s_mov_b32 m0, s52
	v_add_u32_e32 v172, s87, v172
	global_load_lds_dwordx4 v172, s[6:7]
	v_mov_b32_e32 v172, v177
	s_add_i32 s87, s87, s48
	v_add_u32_e32 v172, s87, v172
	s_mov_b32 m0, s53
	s_nop 0
	global_load_lds_dwordx4 v172, s[6:7]
	v_mov_b32_e32 v172, v176
	s_mov_b32 m0, s49
	v_add_u32_e32 v172, s86, v172
	global_load_lds_dwordx4 v172, s[4:5]
	v_mov_b32_e32 v172, v176
	s_add_i32 s86, s86, s47
	v_add_u32_e32 v172, s86, v172
	s_mov_b32 m0, s54
	s_nop 0
	global_load_lds_dwordx4 v172, s[4:5]
	s_waitcnt vmcnt(8)
	s_waitcnt lgkmcnt(0)
	s_barrier
	s_setprio 1
	s_waitcnt lgkmcnt(0)
	v_mfma_f32_16x16x128_f8f6f4 v[94:97], v[18:25], v[164:171], 0
	v_mfma_f32_16x16x128_f8f6f4 v[90:93], v[26:33], v[164:171], 0
	v_mfma_f32_16x16x128_f8f6f4 v[86:89], v[18:25], v[198:205], 0
	v_mfma_f32_16x16x128_f8f6f4 v[82:85], v[26:33], v[198:205], 0
	v_mfma_f32_16x16x128_f8f6f4 v[74:77], v[18:25], v[214:221], 0
	v_mfma_f32_16x16x128_f8f6f4 v[66:69], v[26:33], v[214:221], 0
	v_mfma_f32_16x16x128_f8f6f4 v[58:61], v[18:25], v[222:229], 0
	v_mfma_f32_16x16x128_f8f6f4 v[50:53], v[26:33], v[222:229], 0
	s_setprio 0
	s_setprio 1
	v_mfma_f32_16x16x128_f8f6f4 v[78:81], v[2:9], v[164:171], 0
	v_mfma_f32_16x16x128_f8f6f4 v[70:73], v[10:17], v[164:171], 0
	v_mfma_f32_16x16x128_f8f6f4 v[62:65], v[2:9], v[198:205], 0
	v_mfma_f32_16x16x128_f8f6f4 v[54:57], v[10:17], v[198:205], 0
	v_mfma_f32_16x16x128_f8f6f4 v[46:49], v[2:9], v[214:221], 0
	v_mfma_f32_16x16x128_f8f6f4 v[42:45], v[10:17], v[214:221], 0
	v_mfma_f32_16x16x128_f8f6f4 v[38:41], v[2:9], v[222:229], 0
	v_mfma_f32_16x16x128_f8f6f4 v[34:37], v[10:17], v[222:229], 0
	s_setprio 0
	s_barrier
	s_cmp_lg_u64 s[2:3], 0
	s_cbranch_scc0 .Ltx23_skip_p
	v_readfirstlane_b32 s23, v209
	s_mul_i32 s23, s23, 44
	s_add_i32 s23, s23, s79
	s_lshl_b32 s23, s23, 19
	s_mov_b32 s29, s23
.Ltx23_skip_p:
	ds_read_b128 v[2:5], v184
	ds_read_b128 v[6:9], v185
	ds_read_b128 v[10:13], v192
	ds_read_b128 v[14:17], v193
	ds_read_b128 v[18:21], v186
	ds_read_b128 v[22:25], v187
	ds_read_b128 v[26:29], v194
	ds_read_b128 v[30:33], v195
	v_mov_b32_e32 v172, v176
	ds_read_b128 v[164:167], v196 offset:32768
	ds_read_b128 v[168:171], v196 offset:33792
	ds_read_b128 v[198:201], v196 offset:34816
	ds_read_b128 v[202:205], v196 offset:35840
	ds_read_b128 v[214:217], v196 offset:36864
	ds_read_b128 v[218:221], v196 offset:37888
	ds_read_b128 v[222:225], v196 offset:38912
	ds_read_b128 v[226:229], v196 offset:39936
	s_add_i32 s86, s86, s47
	s_mov_b32 m0, s55
	v_add_u32_e32 v172, s86, v172
	global_load_lds_dwordx4 v172, s[4:5]
	v_mov_b32_e32 v172, v176
	s_add_i32 s86, s86, s47
	v_add_u32_e32 v172, s86, v172
	s_mov_b32 m0, s56
	s_nop 0
	global_load_lds_dwordx4 v172, s[4:5]
	s_waitcnt vmcnt(8)
	s_waitcnt lgkmcnt(0)
	s_barrier
	s_setprio 1
	s_waitcnt lgkmcnt(0)
	v_mfma_f32_16x16x128_f8f6f4 v[158:161], v[2:9], v[164:171], v[158:161]
	v_mfma_f32_16x16x128_f8f6f4 v[154:157], v[10:17], v[164:171], v[154:157]
	v_mfma_f32_16x16x128_f8f6f4 v[150:153], v[2:9], v[198:205], v[150:153]
	v_mfma_f32_16x16x128_f8f6f4 v[146:149], v[10:17], v[198:205], v[146:149]
	v_mfma_f32_16x16x128_f8f6f4 v[138:141], v[2:9], v[214:221], v[138:141]
	v_mfma_f32_16x16x128_f8f6f4 v[130:133], v[10:17], v[214:221], v[130:133]
	v_mfma_f32_16x16x128_f8f6f4 v[122:125], v[2:9], v[222:229], v[122:125]
	v_mfma_f32_16x16x128_f8f6f4 v[114:117], v[10:17], v[222:229], v[114:117]
	s_setprio 0
	s_setprio 1
	v_mfma_f32_16x16x128_f8f6f4 v[142:145], v[18:25], v[164:171], v[142:145]
	v_mfma_f32_16x16x128_f8f6f4 v[134:137], v[26:33], v[164:171], v[134:137]
	v_mfma_f32_16x16x128_f8f6f4 v[126:129], v[18:25], v[198:205], v[126:129]
	v_mfma_f32_16x16x128_f8f6f4 v[118:121], v[26:33], v[198:205], v[118:121]
	v_mfma_f32_16x16x128_f8f6f4 v[110:113], v[18:25], v[214:221], v[110:113]
	v_mfma_f32_16x16x128_f8f6f4 v[106:109], v[26:33], v[214:221], v[106:109]
	v_mfma_f32_16x16x128_f8f6f4 v[102:105], v[18:25], v[222:229], v[102:105]
	v_mfma_f32_16x16x128_f8f6f4 v[98:101], v[26:33], v[222:229], v[98:101]
	s_setprio 0
	s_barrier
	s_branch .Lmid_10
.Lsk23_first:
	ds_read_b128 v[18:21], v180
	ds_read_b128 v[22:25], v181
	ds_read_b128 v[26:29], v188
	ds_read_b128 v[30:33], v189
	ds_read_b128 v[2:5], v182
	ds_read_b128 v[6:9], v183
	ds_read_b128 v[10:13], v190
	ds_read_b128 v[14:17], v191
	s_add_i32 s84, s28, 0x80
	s_cmp_eq_u32 s67, s83
	s_cselect_b32 s86, s25, s84
	s_cselect_b32 s87, s29, s82
	s_add_i32 s84, s86, 0x80
	s_add_i32 s85, s87, 0x80
	v_mov_b32_e32 v172, v176
	ds_read_b128 v[164:167], v196
	ds_read_b128 v[168:171], v196 offset:1024
	ds_read_b128 v[198:201], v196 offset:2048
	ds_read_b128 v[202:205], v196 offset:3072
	ds_read_b128 v[214:217], v196 offset:4096
	ds_read_b128 v[218:221], v196 offset:5120
	ds_read_b128 v[222:225], v196 offset:6144
	ds_read_b128 v[226:229], v196 offset:7168
	s_add_i32 s88, s28, s65
	v_add_u32_e32 v172, s88, v172
	s_add_i32 m0, s49, 0xc000
	s_add_i32 s88, s28, s70
	global_load_lds_dwordx4 v172, s[4:5]
	v_mov_b32_e32 v172, v176
	s_add_i32 m0, s49, 0xe000
	v_add_u32_e32 v172, s88, v172
	global_load_lds_dwordx4 v172, s[4:5]
	v_pk_fma_f32 v[94:95], v[94:95], s[18:19], 0 op_sel_hi:[1,0,0]
	v_pk_fma_f32 v[96:97], v[96:97], s[18:19], 0 op_sel_hi:[1,0,0]
	v_pk_fma_f32 v[90:91], v[90:91], s[18:19], 0 op_sel_hi:[1,0,0]
	v_pk_fma_f32 v[92:93], v[92:93], s[18:19], 0 op_sel_hi:[1,0,0]
	v_pk_fma_f32 v[78:79], v[78:79], s[20:21], 0 op_sel_hi:[1,0,0]
	v_pk_fma_f32 v[80:81], v[80:81], s[20:21], 0 op_sel_hi:[1,0,0]
	v_pk_fma_f32 v[70:71], v[70:71], s[20:21], 0 op_sel_hi:[1,0,0]
	v_pk_fma_f32 v[72:73], v[72:73], s[20:21], 0 op_sel_hi:[1,0,0]
	v_pk_fma_f32 v[86:87], v[86:87], s[18:19], 0 op_sel_hi:[1,0,0]
	v_pk_fma_f32 v[88:89], v[88:89], s[18:19], 0 op_sel_hi:[1,0,0]
	v_pk_fma_f32 v[82:83], v[82:83], s[18:19], 0 op_sel_hi:[1,0,0]
	v_pk_fma_f32 v[84:85], v[84:85], s[18:19], 0 op_sel_hi:[1,0,0]
	v_pk_fma_f32 v[62:63], v[62:63], s[20:21], 0 op_sel_hi:[1,0,0]
	v_pk_fma_f32 v[64:65], v[64:65], s[20:21], 0 op_sel_hi:[1,0,0]
	v_pk_fma_f32 v[54:55], v[54:55], s[20:21], 0 op_sel_hi:[1,0,0]
	v_pk_fma_f32 v[56:57], v[56:57], s[20:21], 0 op_sel_hi:[1,0,0]
	v_pk_mul_f32 v[230:231], v[94:95], s[98:99] op_sel_hi:[1,0]
	v_pk_mul_f32 v[232:233], v[96:97], s[98:99] op_sel_hi:[1,0]
	v_pk_mul_f32 v[234:235], v[90:91], s[98:99] op_sel_hi:[1,0]
	v_pk_mul_f32 v[236:237], v[92:93], s[98:99] op_sel_hi:[1,0]
	v_pk_mul_f32 v[238:239], v[86:87], s[98:99] op_sel_hi:[1,0]
	v_pk_mul_f32 v[240:241], v[88:89], s[98:99] op_sel_hi:[1,0]
	v_pk_mul_f32 v[242:243], v[82:83], s[98:99] op_sel_hi:[1,0]
	v_pk_mul_f32 v[244:245], v[84:85], s[98:99] op_sel_hi:[1,0]
	v_exp_f32_e32 v230, v230
	v_exp_f32_e32 v231, v231
	v_exp_f32_e32 v232, v232
	v_exp_f32_e32 v233, v233
	v_exp_f32_e32 v234, v234
	v_exp_f32_e32 v235, v235
	v_exp_f32_e32 v236, v236
	v_exp_f32_e32 v237, v237
	v_exp_f32_e32 v238, v238
	v_exp_f32_e32 v239, v239
	v_exp_f32_e32 v240, v240
	v_exp_f32_e32 v241, v241
	v_exp_f32_e32 v242, v242
	v_exp_f32_e32 v243, v243
	v_exp_f32_e32 v244, v244
	v_exp_f32_e32 v245, v245
	v_pk_add_f32 v[230:231], v[230:231], 1.0 op_sel_hi:[1,0]
	v_pk_add_f32 v[232:233], v[232:233], 1.0 op_sel_hi:[1,0]
	v_pk_add_f32 v[234:235], v[234:235], 1.0 op_sel_hi:[1,0]
	v_pk_add_f32 v[236:237], v[236:237], 1.0 op_sel_hi:[1,0]
	v_pk_add_f32 v[238:239], v[238:239], 1.0 op_sel_hi:[1,0]
	v_pk_add_f32 v[240:241], v[240:241], 1.0 op_sel_hi:[1,0]
	v_pk_add_f32 v[242:243], v[242:243], 1.0 op_sel_hi:[1,0]
	v_pk_add_f32 v[244:245], v[244:245], 1.0 op_sel_hi:[1,0]
	v_rcp_f32_e32 v230, v230
	v_rcp_f32_e32 v231, v231
	v_rcp_f32_e32 v232, v232
	v_rcp_f32_e32 v233, v233
	v_rcp_f32_e32 v234, v234
	v_rcp_f32_e32 v235, v235
	v_rcp_f32_e32 v236, v236
	v_rcp_f32_e32 v237, v237
	v_rcp_f32_e32 v238, v238
	v_rcp_f32_e32 v239, v239
	v_rcp_f32_e32 v240, v240
	v_rcp_f32_e32 v241, v241
	v_rcp_f32_e32 v242, v242
	v_rcp_f32_e32 v243, v243
	v_rcp_f32_e32 v244, v244
	v_rcp_f32_e32 v245, v245
	v_pk_mul_f32 v[230:231], v[94:95], v[230:231]
	v_pk_mul_f32 v[232:233], v[96:97], v[232:233]
	v_pk_mul_f32 v[234:235], v[90:91], v[234:235]
	v_pk_mul_f32 v[236:237], v[92:93], v[236:237]
	v_pk_mul_f32 v[238:239], v[86:87], v[238:239]
	v_pk_mul_f32 v[240:241], v[88:89], v[240:241]
	v_pk_mul_f32 v[242:243], v[82:83], v[242:243]
	v_pk_mul_f32 v[244:245], v[84:85], v[244:245]
	v_pk_mul_f32 v[78:79], v[78:79], v[230:231]
	v_pk_mul_f32 v[80:81], v[80:81], v[232:233]
	v_pk_mul_f32 v[70:71], v[70:71], v[234:235]
	v_pk_mul_f32 v[72:73], v[72:73], v[236:237]
	v_pk_mul_f32 v[62:63], v[62:63], v[238:239]
	v_pk_mul_f32 v[64:65], v[64:65], v[240:241]
	v_pk_mul_f32 v[54:55], v[54:55], v[242:243]
	v_pk_mul_f32 v[56:57], v[56:57], v[244:245]
	v_med3_f32 v78, v78, s72, v197
	v_med3_f32 v79, v79, s72, v197
	v_med3_f32 v80, v80, s72, v197
	v_med3_f32 v81, v81, s72, v197
	v_med3_f32 v70, v70, s72, v197
	v_med3_f32 v71, v71, s72, v197
	v_med3_f32 v72, v72, s72, v197
	v_med3_f32 v73, v73, s72, v197
	v_med3_f32 v62, v62, s72, v197
	v_med3_f32 v63, v63, s72, v197
	v_med3_f32 v64, v64, s72, v197
	v_med3_f32 v65, v65, s72, v197
	v_med3_f32 v54, v54, s72, v197
	v_med3_f32 v55, v55, s72, v197
	v_med3_f32 v56, v56, s72, v197
	v_med3_f32 v57, v57, s72, v197
	v_cvt_pk_fp8_f32 v246, v78, v79
	v_cvt_pk_fp8_f32 v247, v70, v71
	v_cvt_pk_fp8_f32 v248, v62, v63
	v_cvt_pk_fp8_f32 v249, v54, v55
	v_add_u32_e32 v207, s75, v206
	v_add_u32_e32 v208, s76, v206
	v_cvt_pk_fp8_f32 v246, v80, v81 op_sel:[0,0,1]
	v_cvt_pk_fp8_f32 v247, v72, v73 op_sel:[0,0,1]
	v_cvt_pk_fp8_f32 v248, v64, v65 op_sel:[0,0,1]
	v_cvt_pk_fp8_f32 v249, v56, v57 op_sel:[0,0,1]
	s_nop 1
	global_store_dwordx2 v207, v[246:247], s[100:101]
	global_store_dwordx2 v208, v[248:249], s[100:101]
	s_waitcnt vmcnt(10)
	s_waitcnt lgkmcnt(0)
	s_barrier
	s_setprio 1
	s_waitcnt lgkmcnt(0)
	v_mfma_f32_16x16x128_f8f6f4 v[158:161], v[18:25], v[164:171], 0
	v_pk_fma_f32 v[74:75], v[74:75], s[18:19], 0 op_sel_hi:[1,0,0]
	v_pk_fma_f32 v[76:77], v[76:77], s[18:19], 0 op_sel_hi:[1,0,0]
	v_pk_fma_f32 v[66:67], v[66:67], s[18:19], 0 op_sel_hi:[1,0,0]
	v_pk_fma_f32 v[68:69], v[68:69], s[18:19], 0 op_sel_hi:[1,0,0]
	v_pk_fma_f32 v[46:47], v[46:47], s[20:21], 0 op_sel_hi:[1,0,0]
	v_pk_fma_f32 v[48:49], v[48:49], s[20:21], 0 op_sel_hi:[1,0,0]
	v_pk_fma_f32 v[42:43], v[42:43], s[20:21], 0 op_sel_hi:[1,0,0]
	v_mfma_f32_16x16x128_f8f6f4 v[154:157], v[26:33], v[164:171], 0
	v_pk_fma_f32 v[44:45], v[44:45], s[20:21], 0 op_sel_hi:[1,0,0]
	v_pk_fma_f32 v[58:59], v[58:59], s[18:19], 0 op_sel_hi:[1,0,0]
	v_pk_fma_f32 v[60:61], v[60:61], s[18:19], 0 op_sel_hi:[1,0,0]
	v_pk_fma_f32 v[50:51], v[50:51], s[18:19], 0 op_sel_hi:[1,0,0]
	v_pk_fma_f32 v[52:53], v[52:53], s[18:19], 0 op_sel_hi:[1,0,0]
	v_pk_fma_f32 v[38:39], v[38:39], s[20:21], 0 op_sel_hi:[1,0,0]
	v_pk_fma_f32 v[40:41], v[40:41], s[20:21], 0 op_sel_hi:[1,0,0]
	v_mfma_f32_16x16x128_f8f6f4 v[150:153], v[18:25], v[198:205], 0
	v_pk_fma_f32 v[34:35], v[34:35], s[20:21], 0 op_sel_hi:[1,0,0]
	v_pk_fma_f32 v[36:37], v[36:37], s[20:21], 0 op_sel_hi:[1,0,0]
	v_pk_mul_f32 v[230:231], v[74:75], s[98:99] op_sel_hi:[1,0]
	v_pk_mul_f32 v[232:233], v[76:77], s[98:99] op_sel_hi:[1,0]
	v_pk_mul_f32 v[234:235], v[66:67], s[98:99] op_sel_hi:[1,0]
	v_pk_mul_f32 v[236:237], v[68:69], s[98:99] op_sel_hi:[1,0]
	v_pk_mul_f32 v[238:239], v[58:59], s[98:99] op_sel_hi:[1,0]
	v_mfma_f32_16x16x128_f8f6f4 v[146:149], v[26:33], v[198:205], 0
	v_pk_mul_f32 v[240:241], v[60:61], s[98:99] op_sel_hi:[1,0]
	v_pk_mul_f32 v[242:243], v[50:51], s[98:99] op_sel_hi:[1,0]
	v_pk_mul_f32 v[244:245], v[52:53], s[98:99] op_sel_hi:[1,0]
	v_exp_f32_e32 v230, v230
	v_exp_f32_e32 v231, v231
	v_exp_f32_e32 v232, v232
	v_exp_f32_e32 v233, v233
	v_mfma_f32_16x16x128_f8f6f4 v[138:141], v[18:25], v[214:221], 0
	v_exp_f32_e32 v234, v234
	v_exp_f32_e32 v235, v235
	v_exp_f32_e32 v236, v236
	v_exp_f32_e32 v237, v237
	v_exp_f32_e32 v238, v238
	v_exp_f32_e32 v239, v239
	v_exp_f32_e32 v240, v240
	v_mfma_f32_16x16x128_f8f6f4 v[130:133], v[26:33], v[214:221], 0
	v_exp_f32_e32 v241, v241
	v_exp_f32_e32 v242, v242
	v_exp_f32_e32 v243, v243
	v_exp_f32_e32 v244, v244
	v_exp_f32_e32 v245, v245
	v_pk_add_f32 v[230:231], v[230:231], 1.0 op_sel_hi:[1,0]
	v_pk_add_f32 v[232:233], v[232:233], 1.0 op_sel_hi:[1,0]
	v_mfma_f32_16x16x128_f8f6f4 v[122:125], v[18:25], v[222:229], 0
	v_pk_add_f32 v[234:235], v[234:235], 1.0 op_sel_hi:[1,0]
	v_pk_add_f32 v[236:237], v[236:237], 1.0 op_sel_hi:[1,0]
	v_pk_add_f32 v[238:239], v[238:239], 1.0 op_sel_hi:[1,0]
	v_pk_add_f32 v[240:241], v[240:241], 1.0 op_sel_hi:[1,0]
	v_pk_add_f32 v[242:243], v[242:243], 1.0 op_sel_hi:[1,0]
	v_pk_add_f32 v[244:245], v[244:245], 1.0 op_sel_hi:[1,0]
	v_rcp_f32_e32 v230, v230
	v_mfma_f32_16x16x128_f8f6f4 v[114:117], v[26:33], v[222:229], 0
	v_rcp_f32_e32 v231, v231
	v_rcp_f32_e32 v232, v232
	v_rcp_f32_e32 v233, v233
	v_rcp_f32_e32 v234, v234
	v_rcp_f32_e32 v235, v235
	v_rcp_f32_e32 v236, v236
	v_rcp_f32_e32 v237, v237
	s_setprio 0
	s_setprio 1
	v_mfma_f32_16x16x128_f8f6f4 v[142:145], v[2:9], v[164:171], 0
	v_rcp_f32_e32 v238, v238
	v_rcp_f32_e32 v239, v239
	v_rcp_f32_e32 v240, v240
	v_rcp_f32_e32 v241, v241
	v_rcp_f32_e32 v242, v242
	v_rcp_f32_e32 v243, v243
	v_rcp_f32_e32 v244, v244
	v_mfma_f32_16x16x128_f8f6f4 v[134:137], v[10:17], v[164:171], 0
	v_rcp_f32_e32 v245, v245
	v_pk_mul_f32 v[230:231], v[74:75], v[230:231]
	v_pk_mul_f32 v[232:233], v[76:77], v[232:233]
	v_pk_mul_f32 v[234:235], v[66:67], v[234:235]
	v_pk_mul_f32 v[236:237], v[68:69], v[236:237]
	v_pk_mul_f32 v[238:239], v[58:59], v[238:239]
	v_pk_mul_f32 v[240:241], v[60:61], v[240:241]
	v_mfma_f32_16x16x128_f8f6f4 v[126:129], v[2:9], v[198:205], 0
	v_pk_mul_f32 v[242:243], v[50:51], v[242:243]
	v_pk_mul_f32 v[244:245], v[52:53], v[244:245]
	v_pk_mul_f32 v[46:47], v[46:47], v[230:231]
	v_pk_mul_f32 v[48:49], v[48:49], v[232:233]
	v_pk_mul_f32 v[42:43], v[42:43], v[234:235]
	v_pk_mul_f32 v[44:45], v[44:45], v[236:237]
	v_pk_mul_f32 v[38:39], v[38:39], v[238:239]
	v_mfma_f32_16x16x128_f8f6f4 v[118:121], v[10:17], v[198:205], 0
	v_pk_mul_f32 v[40:41], v[40:41], v[240:241]
	v_pk_mul_f32 v[34:35], v[34:35], v[242:243]
	v_pk_mul_f32 v[36:37], v[36:37], v[244:245]
	v_med3_f32 v46, v46, s72, v197
	v_med3_f32 v47, v47, s72, v197
	v_med3_f32 v48, v48, s72, v197
	v_med3_f32 v49, v49, s72, v197
	v_mfma_f32_16x16x128_f8f6f4 v[110:113], v[2:9], v[214:221], 0
	v_med3_f32 v42, v42, s72, v197
	v_med3_f32 v43, v43, s72, v197
	v_med3_f32 v44, v44, s72, v197
	v_med3_f32 v45, v45, s72, v197
	v_med3_f32 v38, v38, s72, v197
	v_med3_f32 v39, v39, s72, v197
	v_med3_f32 v40, v40, s72, v197
	v_mfma_f32_16x16x128_f8f6f4 v[106:109], v[10:17], v[214:221], 0
	v_med3_f32 v41, v41, s72, v197
	v_med3_f32 v34, v34, s72, v197
	v_med3_f32 v35, v35, s72, v197
	v_med3_f32 v36, v36, s72, v197
	v_med3_f32 v37, v37, s72, v197
	v_cvt_pk_fp8_f32 v246, v46, v47
	v_cvt_pk_fp8_f32 v247, v42, v43
	v_mfma_f32_16x16x128_f8f6f4 v[102:105], v[2:9], v[222:229], 0
	v_cvt_pk_fp8_f32 v248, v38, v39
	v_cvt_pk_fp8_f32 v249, v34, v35
	v_add_u32_e32 v207, s77, v206
	v_add_u32_e32 v208, 0xf2000, v206
	v_cvt_pk_fp8_f32 v246, v48, v49 op_sel:[0,0,1]
	v_cvt_pk_fp8_f32 v247, v44, v45 op_sel:[0,0,1]
	v_cvt_pk_fp8_f32 v248, v40, v41 op_sel:[0,0,1]
	v_mfma_f32_16x16x128_f8f6f4 v[98:101], v[10:17], v[222:229], 0
	v_cvt_pk_fp8_f32 v249, v36, v37 op_sel:[0,0,1]
	s_nop 1
	global_store_dwordx2 v207, v[246:247], s[100:101]
	global_store_dwordx2 v208, v[248:249], s[100:101]
	s_setprio 0
	s_barrier
	v_mov_b32_e32 v172, v177
	ds_read_b128 v[164:167], v196 offset:16384
	ds_read_b128 v[168:171], v196 offset:17408
	ds_read_b128 v[198:201], v196 offset:18432
	ds_read_b128 v[202:205], v196 offset:19456
	ds_read_b128 v[214:217], v196 offset:20480
	ds_read_b128 v[218:221], v196 offset:21504
	ds_read_b128 v[222:225], v196 offset:22528
	ds_read_b128 v[226:229], v196 offset:23552
	s_mov_b32 m0, s50
	v_add_u32_e32 v172, s87, v172
	global_load_lds_dwordx4 v172, s[6:7]
	v_mov_b32_e32 v172, v177
	s_add_i32 s87, s87, s48
	v_add_u32_e32 v172, s87, v172
	s_mov_b32 m0, s51
	s_add_i32 s87, s87, s48
	global_load_lds_dwordx4 v172, s[6:7]
	v_mov_b32_e32 v172, v177
	s_mov_b32 m0, s52
	v_add_u32_e32 v172, s87, v172
	global_load_lds_dwordx4 v172, s[6:7]
	v_mov_b32_e32 v172, v177
	s_add_i32 s87, s87, s48
	v_add_u32_e32 v172, s87, v172
	s_mov_b32 m0, s53
	s_nop 0
	global_load_lds_dwordx4 v172, s[6:7]
	v_mov_b32_e32 v172, v176
	s_mov_b32 m0, s49
	v_add_u32_e32 v172, s86, v172
	global_load_lds_dwordx4 v172, s[4:5]
	v_mov_b32_e32 v172, v176
	s_add_i32 s86, s86, s47
	v_add_u32_e32 v172, s86, v172
	s_mov_b32 m0, s54
	s_nop 0
	global_load_lds_dwordx4 v172, s[4:5]
	s_waitcnt vmcnt(12)
	s_waitcnt lgkmcnt(0)
	s_barrier
	s_setprio 1
	s_waitcnt lgkmcnt(0)
	v_mfma_f32_16x16x128_f8f6f4 v[94:97], v[18:25], v[164:171], 0
	v_mfma_f32_16x16x128_f8f6f4 v[90:93], v[26:33], v[164:171], 0
	v_mfma_f32_16x16x128_f8f6f4 v[86:89], v[18:25], v[198:205], 0
	v_mfma_f32_16x16x128_f8f6f4 v[82:85], v[26:33], v[198:205], 0
	v_mfma_f32_16x16x128_f8f6f4 v[74:77], v[18:25], v[214:221], 0
	v_mfma_f32_16x16x128_f8f6f4 v[66:69], v[26:33], v[214:221], 0
	v_mfma_f32_16x16x128_f8f6f4 v[58:61], v[18:25], v[222:229], 0
	v_mfma_f32_16x16x128_f8f6f4 v[50:53], v[26:33], v[222:229], 0
	s_setprio 0
	s_setprio 1
	v_mfma_f32_16x16x128_f8f6f4 v[78:81], v[2:9], v[164:171], 0
	v_mfma_f32_16x16x128_f8f6f4 v[70:73], v[10:17], v[164:171], 0
	v_mfma_f32_16x16x128_f8f6f4 v[62:65], v[2:9], v[198:205], 0
	v_mfma_f32_16x16x128_f8f6f4 v[54:57], v[10:17], v[198:205], 0
	v_mfma_f32_16x16x128_f8f6f4 v[46:49], v[2:9], v[214:221], 0
	v_mfma_f32_16x16x128_f8f6f4 v[42:45], v[10:17], v[214:221], 0
	v_mfma_f32_16x16x128_f8f6f4 v[38:41], v[2:9], v[222:229], 0
	v_mfma_f32_16x16x128_f8f6f4 v[34:37], v[10:17], v[222:229], 0
	s_setprio 0
	s_barrier
	s_cmp_lg_u64 s[2:3], 0
	s_cbranch_scc0 .Ltx23_skip_s
	v_readfirstlane_b32 s23, v209
	s_mul_i32 s23, s23, 44
	s_add_i32 s23, s23, s79
	s_lshl_b32 s23, s23, 19
	s_mov_b32 s29, s23
.Ltx23_skip_s:
	ds_read_b128 v[2:5], v184
	ds_read_b128 v[6:9], v185
	ds_read_b128 v[10:13], v192
	ds_read_b128 v[14:17], v193
	ds_read_b128 v[18:21], v186
	ds_read_b128 v[22:25], v187
	ds_read_b128 v[26:29], v194
	ds_read_b128 v[30:33], v195
	v_mov_b32_e32 v172, v176
	ds_read_b128 v[164:167], v196 offset:32768
	ds_read_b128 v[168:171], v196 offset:33792
	ds_read_b128 v[198:201], v196 offset:34816
	ds_read_b128 v[202:205], v196 offset:35840
	ds_read_b128 v[214:217], v196 offset:36864
	ds_read_b128 v[218:221], v196 offset:37888
	ds_read_b128 v[222:225], v196 offset:38912
	ds_read_b128 v[226:229], v196 offset:39936
	s_add_i32 s86, s86, s47
	s_mov_b32 m0, s55
	v_add_u32_e32 v172, s86, v172
	global_load_lds_dwordx4 v172, s[4:5]
	v_mov_b32_e32 v172, v176
	s_add_i32 s86, s86, s47
	v_add_u32_e32 v172, s86, v172
	s_mov_b32 m0, s56
	s_nop 0
	global_load_lds_dwordx4 v172, s[4:5]
	s_waitcnt vmcnt(12)
	s_waitcnt lgkmcnt(0)
	s_barrier
	s_setprio 1
	s_waitcnt lgkmcnt(0)
	v_mfma_f32_16x16x128_f8f6f4 v[158:161], v[2:9], v[164:171], v[158:161]
	v_mfma_f32_16x16x128_f8f6f4 v[154:157], v[10:17], v[164:171], v[154:157]
	v_mfma_f32_16x16x128_f8f6f4 v[150:153], v[2:9], v[198:205], v[150:153]
	v_mfma_f32_16x16x128_f8f6f4 v[146:149], v[10:17], v[198:205], v[146:149]
	v_mfma_f32_16x16x128_f8f6f4 v[138:141], v[2:9], v[214:221], v[138:141]
	v_mfma_f32_16x16x128_f8f6f4 v[130:133], v[10:17], v[214:221], v[130:133]
	v_mfma_f32_16x16x128_f8f6f4 v[122:125], v[2:9], v[222:229], v[122:125]
	v_mfma_f32_16x16x128_f8f6f4 v[114:117], v[10:17], v[222:229], v[114:117]
	s_setprio 0
	s_setprio 1
	v_mfma_f32_16x16x128_f8f6f4 v[142:145], v[18:25], v[164:171], v[142:145]
	v_mfma_f32_16x16x128_f8f6f4 v[134:137], v[26:33], v[164:171], v[134:137]
	v_mfma_f32_16x16x128_f8f6f4 v[126:129], v[18:25], v[198:205], v[126:129]
	v_mfma_f32_16x16x128_f8f6f4 v[118:121], v[26:33], v[198:205], v[118:121]
	v_mfma_f32_16x16x128_f8f6f4 v[110:113], v[18:25], v[214:221], v[110:113]
	v_mfma_f32_16x16x128_f8f6f4 v[106:109], v[26:33], v[214:221], v[106:109]
	v_mfma_f32_16x16x128_f8f6f4 v[102:105], v[18:25], v[222:229], v[102:105]
	v_mfma_f32_16x16x128_f8f6f4 v[98:101], v[26:33], v[222:229], v[98:101]
	s_setprio 0
	s_barrier
	s_mov_b32 s99, 0
	s_branch .Lmid_10
.LBB0_2937:
	ds_read_b128 v[18:21], v180
	ds_read_b128 v[22:25], v181
	ds_read_b128 v[26:29], v188
	ds_read_b128 v[30:33], v189
	ds_read_b128 v[2:5], v182
	ds_read_b128 v[6:9], v183
	ds_read_b128 v[10:13], v190
	ds_read_b128 v[14:17], v191
	s_add_i32 s84, s28, 0x80
	s_cmp_eq_u32 s67, s83
	s_cselect_b32 s86, s25, s84
	s_cselect_b32 s87, s29, s82
	s_add_i32 s84, s86, 0x80
	s_add_i32 s85, s87, 0x80
	v_mov_b32_e32 v172, v176
	ds_read_b128 v[164:167], v196
	ds_read_b128 v[168:171], v196 offset:1024
	ds_read_b128 v[198:201], v196 offset:2048
	ds_read_b128 v[202:205], v196 offset:3072
	ds_read_b128 v[214:217], v196 offset:4096
	ds_read_b128 v[218:221], v196 offset:5120
	ds_read_b128 v[222:225], v196 offset:6144
	ds_read_b128 v[226:229], v196 offset:7168
	s_add_i32 s88, s28, s65
	v_add_u32_e32 v172, s88, v172
	s_add_i32 m0, s49, 0xc000
	s_add_i32 s88, s28, s70
	global_load_lds_dwordx4 v172, s[4:5]
	v_mov_b32_e32 v172, v176
	s_add_i32 m0, s49, 0xe000
	v_add_u32_e32 v172, s88, v172
	global_load_lds_dwordx4 v172, s[4:5]
	s_waitcnt vmcnt(8)
	s_waitcnt lgkmcnt(0)
	s_barrier
	s_setprio 1
	s_waitcnt lgkmcnt(0)
	v_mfma_f32_16x16x128_f8f6f4 v[158:161], v[18:25], v[164:171], v[158:161]
	v_mfma_f32_16x16x128_f8f6f4 v[154:157], v[26:33], v[164:171], v[154:157]
	v_mfma_f32_16x16x128_f8f6f4 v[150:153], v[18:25], v[198:205], v[150:153]
	v_mfma_f32_16x16x128_f8f6f4 v[146:149], v[26:33], v[198:205], v[146:149]
	v_mfma_f32_16x16x128_f8f6f4 v[138:141], v[18:25], v[214:221], v[138:141]
	v_mfma_f32_16x16x128_f8f6f4 v[130:133], v[26:33], v[214:221], v[130:133]
	v_mfma_f32_16x16x128_f8f6f4 v[122:125], v[18:25], v[222:229], v[122:125]
	v_mfma_f32_16x16x128_f8f6f4 v[114:117], v[26:33], v[222:229], v[114:117]
	s_setprio 0
	s_setprio 1
	v_mfma_f32_16x16x128_f8f6f4 v[142:145], v[2:9], v[164:171], v[142:145]
	v_mfma_f32_16x16x128_f8f6f4 v[134:137], v[10:17], v[164:171], v[134:137]
	v_mfma_f32_16x16x128_f8f6f4 v[126:129], v[2:9], v[198:205], v[126:129]
	v_mfma_f32_16x16x128_f8f6f4 v[118:121], v[10:17], v[198:205], v[118:121]
	v_mfma_f32_16x16x128_f8f6f4 v[110:113], v[2:9], v[214:221], v[110:113]
	v_mfma_f32_16x16x128_f8f6f4 v[106:109], v[10:17], v[214:221], v[106:109]
	v_mfma_f32_16x16x128_f8f6f4 v[102:105], v[2:9], v[222:229], v[102:105]
	v_mfma_f32_16x16x128_f8f6f4 v[98:101], v[10:17], v[222:229], v[98:101]
	s_setprio 0
	s_barrier
	v_mov_b32_e32 v172, v177
	ds_read_b128 v[164:167], v196 offset:16384
	ds_read_b128 v[168:171], v196 offset:17408
	ds_read_b128 v[198:201], v196 offset:18432
	ds_read_b128 v[202:205], v196 offset:19456
	ds_read_b128 v[214:217], v196 offset:20480
	ds_read_b128 v[218:221], v196 offset:21504
	ds_read_b128 v[222:225], v196 offset:22528
	ds_read_b128 v[226:229], v196 offset:23552
	s_mov_b32 m0, s50
	v_add_u32_e32 v172, s87, v172
	global_load_lds_dwordx4 v172, s[6:7]
	v_mov_b32_e32 v172, v177
	s_add_i32 s87, s87, s48
	v_add_u32_e32 v172, s87, v172
	s_mov_b32 m0, s51
	s_add_i32 s87, s87, s48
	global_load_lds_dwordx4 v172, s[6:7]
	v_mov_b32_e32 v172, v177
	s_mov_b32 m0, s52
	v_add_u32_e32 v172, s87, v172
	global_load_lds_dwordx4 v172, s[6:7]
	v_mov_b32_e32 v172, v177
	s_add_i32 s87, s87, s48
	v_add_u32_e32 v172, s87, v172
	s_mov_b32 m0, s53
	s_nop 0
	global_load_lds_dwordx4 v172, s[6:7]
	v_mov_b32_e32 v172, v176
	s_mov_b32 m0, s49
	v_add_u32_e32 v172, s86, v172
	global_load_lds_dwordx4 v172, s[4:5]
	v_mov_b32_e32 v172, v176
	s_add_i32 s86, s86, s47
	v_add_u32_e32 v172, s86, v172
	s_mov_b32 m0, s54
	s_nop 0
	global_load_lds_dwordx4 v172, s[4:5]
	s_waitcnt vmcnt(8)
	s_waitcnt lgkmcnt(0)
	s_barrier
	s_setprio 1
	s_waitcnt lgkmcnt(0)
	v_mfma_f32_16x16x128_f8f6f4 v[94:97], v[18:25], v[164:171], v[94:97]
	v_mfma_f32_16x16x128_f8f6f4 v[90:93], v[26:33], v[164:171], v[90:93]
	v_mfma_f32_16x16x128_f8f6f4 v[86:89], v[18:25], v[198:205], v[86:89]
	v_mfma_f32_16x16x128_f8f6f4 v[82:85], v[26:33], v[198:205], v[82:85]
	v_mfma_f32_16x16x128_f8f6f4 v[74:77], v[18:25], v[214:221], v[74:77]
	v_mfma_f32_16x16x128_f8f6f4 v[66:69], v[26:33], v[214:221], v[66:69]
	v_mfma_f32_16x16x128_f8f6f4 v[58:61], v[18:25], v[222:229], v[58:61]
	v_mfma_f32_16x16x128_f8f6f4 v[50:53], v[26:33], v[222:229], v[50:53]
	s_setprio 0
	s_setprio 1
	v_mfma_f32_16x16x128_f8f6f4 v[78:81], v[2:9], v[164:171], v[78:81]
	v_mfma_f32_16x16x128_f8f6f4 v[70:73], v[10:17], v[164:171], v[70:73]
	v_mfma_f32_16x16x128_f8f6f4 v[62:65], v[2:9], v[198:205], v[62:65]
	v_mfma_f32_16x16x128_f8f6f4 v[54:57], v[10:17], v[198:205], v[54:57]
	v_mfma_f32_16x16x128_f8f6f4 v[46:49], v[2:9], v[214:221], v[46:49]
	v_mfma_f32_16x16x128_f8f6f4 v[42:45], v[10:17], v[214:221], v[42:45]
	v_mfma_f32_16x16x128_f8f6f4 v[38:41], v[2:9], v[222:229], v[38:41]
	v_mfma_f32_16x16x128_f8f6f4 v[34:37], v[10:17], v[222:229], v[34:37]
	s_setprio 0
	s_barrier
	s_cmp_lg_u64 s[2:3], 0
	s_cbranch_scc0 .Ltx23_skip
	v_readfirstlane_b32 s23, v209
	s_mul_i32 s23, s23, 44
	s_add_i32 s23, s23, s79
	s_lshl_b32 s23, s23, 19
	s_mov_b32 s29, s23

.Lmid_10:
	s_cmp_eq_u32 s67, s83
	s_cbranch_scc1 .Lh23_last
	v_mov_b32_e32 v172, v177
	ds_read_b128 v[164:167], v196 offset:49152
	ds_read_b128 v[168:171], v196 offset:50176
	ds_read_b128 v[198:201], v196 offset:51200
	ds_read_b128 v[202:205], v196 offset:52224
	ds_read_b128 v[214:217], v196 offset:53248
	ds_read_b128 v[218:221], v196 offset:54272
	ds_read_b128 v[222:225], v196 offset:55296
	ds_read_b128 v[226:229], v196 offset:56320
	s_mov_b32 m0, s58
	v_add_u32_e32 v172, s85, v172
	global_load_lds_dwordx4 v172, s[6:7]
	v_mov_b32_e32 v172, v177
	s_add_i32 s85, s85, s48
	v_add_u32_e32 v172, s85, v172
	s_mov_b32 m0, s59
	s_add_i32 s85, s85, s48
	global_load_lds_dwordx4 v172, s[6:7]
	v_mov_b32_e32 v172, v177
	s_mov_b32 m0, s62
	v_add_u32_e32 v172, s85, v172
	global_load_lds_dwordx4 v172, s[6:7]
	v_mov_b32_e32 v172, v177
	s_add_i32 s85, s85, s48
	v_add_u32_e32 v172, s85, v172
	s_mov_b32 m0, s63
	s_nop 0
	global_load_lds_dwordx4 v172, s[6:7]
	v_mov_b32_e32 v172, v176
	s_mov_b32 m0, s60
	v_add_u32_e32 v172, s84, v172
	global_load_lds_dwordx4 v172, s[4:5]
	v_mov_b32_e32 v172, v176
	s_add_i32 s84, s84, s47
	v_add_u32_e32 v172, s84, v172
	s_mov_b32 m0, s61
	s_nop 0
	global_load_lds_dwordx4 v172, s[4:5]
	s_waitcnt vmcnt(8)
	s_waitcnt lgkmcnt(0)
	s_barrier
	s_setprio 1
	s_waitcnt lgkmcnt(0)
	v_mfma_f32_16x16x128_f8f6f4 v[94:97], v[2:9], v[164:171], v[94:97]
	v_mfma_f32_16x16x128_f8f6f4 v[90:93], v[10:17], v[164:171], v[90:93]
	v_mfma_f32_16x16x128_f8f6f4 v[86:89], v[2:9], v[198:205], v[86:89]
	v_mfma_f32_16x16x128_f8f6f4 v[82:85], v[10:17], v[198:205], v[82:85]
	v_mfma_f32_16x16x128_f8f6f4 v[74:77], v[2:9], v[214:221], v[74:77]
	v_mfma_f32_16x16x128_f8f6f4 v[66:69], v[10:17], v[214:221], v[66:69]
	v_mfma_f32_16x16x128_f8f6f4 v[58:61], v[2:9], v[222:229], v[58:61]
	v_mfma_f32_16x16x128_f8f6f4 v[50:53], v[10:17], v[222:229], v[50:53]
	s_setprio 0
	s_setprio 1
	v_mfma_f32_16x16x128_f8f6f4 v[78:81], v[18:25], v[164:171], v[78:81]
	v_mfma_f32_16x16x128_f8f6f4 v[70:73], v[26:33], v[164:171], v[70:73]
	v_mfma_f32_16x16x128_f8f6f4 v[62:65], v[18:25], v[198:205], v[62:65]
	v_mfma_f32_16x16x128_f8f6f4 v[54:57], v[26:33], v[198:205], v[54:57]
	v_mfma_f32_16x16x128_f8f6f4 v[46:49], v[18:25], v[214:221], v[46:49]
	v_mfma_f32_16x16x128_f8f6f4 v[42:45], v[26:33], v[214:221], v[42:45]
	v_mfma_f32_16x16x128_f8f6f4 v[38:41], v[18:25], v[222:229], v[38:41]
	v_mfma_f32_16x16x128_f8f6f4 v[34:37], v[26:33], v[222:229], v[34:37]
	s_setprio 0
	s_barrier
	s_add_i32 s83, s83, 2
	s_addk_i32 s28, 0x100
	s_addk_i32 s82, 0x100
	s_cmp_ge_i32 s83, s64
	s_cbranch_scc0 .LBB0_2937
	s_branch .LBB0_2939

.Lh23_nb:
	s_nop 15
	s_nop 15
	s_cmp_lg_u64 s[2:3], 0
	s_cbranch_scc0 .Lh23_epi1
	s_mov_b32 s99, 1
	s_branch .Lh23_tail

.Lh23_tail:
	s_andn2_b64 vcc, exec, s[2:3]
	s_mov_b64 s[2:3], -1
	s_cbranch_vccnz .LBB0_2928
	s_andn2_b64 vcc, exec, s[10:11]
	s_cbranch_vccnz .LBB0_2927
	s_barrier
	s_branch .LBB0_2927
